# P1 norm1/MoE-combine loop (layers 1-3): entry-path-only waits (header vmcnt(4), mid-iteration vmcnt(0..3)) removed from the back edge, one vmcnt(0) before the loop instead; on top of v9_prohoist
# speedup vs baseline: 1.0025x; 1.0025x over previous
.LBB0_263:
	s_or_b64 exec, exec, s[2:3]
	s_and_saveexec_b64 s[2:3], vcc
	s_cbranch_execz .LBB0_292
	v_mov_b32_e32 v5, v3
	v_lshl_add_u64 v[30:31], s[40:41], 0, v[4:5]
	v_lshl_add_u64 v[32:33], s[42:43], 0, v[4:5]
	v_mov_b32_e32 v7, v3
	v_lshl_add_u64 v[4:5], s[4:5], 0, v[4:5]
	s_mov_b64 s[0:1], 0x1701b000
	v_lshl_add_u64 v[34:35], s[34:35], 0, v[6:7]
	v_lshl_add_u32 v124, v10, 4, 0
	v_lshl_add_u64 v[36:37], v[4:5], 0, s[0:1]
	s_mov_b64 s[34:35], 0
	v_mov_b32_e32 v40, v122
	s_waitcnt vmcnt(0)
	s_branch .LBB0_266

.LBB0_266:
	v_mov_b32_e32 v21, -1
	v_cmp_lt_i32_e32 vcc, -1, v20
	v_mov_b64_e32 v[114:115], 0
	v_mov_b32_e32 v51, 0
	v_mov_b32_e32 v50, 0
	v_mov_b32_e32 v53, 0
	v_mov_b32_e32 v52, 0
	v_mov_b32_e32 v55, 0
	v_mov_b32_e32 v54, 0
	v_mov_b32_e32 v57, 0
	v_mov_b32_e32 v56, 0
	v_mov_b32_e32 v59, 0
	v_mov_b32_e32 v58, 0
	v_mov_b32_e32 v61, 0
	v_mov_b32_e32 v60, 0
	v_mov_b32_e32 v63, 0
	v_mov_b32_e32 v62, 0
	v_mov_b32_e32 v65, 0
	v_mov_b32_e32 v64, 0
	v_mov_b32_e32 v79, 0
	v_mov_b32_e32 v78, 0
	v_mov_b32_e32 v83, 0
	v_mov_b32_e32 v82, 0
	v_mov_b32_e32 v85, 0
	v_mov_b32_e32 v84, 0
	v_mov_b32_e32 v69, 0
	v_mov_b32_e32 v68, 0
	v_mov_b32_e32 v107, 0
	v_mov_b32_e32 v106, 0
	v_mov_b32_e32 v109, 0
	v_mov_b32_e32 v108, 0
	v_mov_b32_e32 v111, 0
	v_mov_b32_e32 v110, 0
	v_mov_b32_e32 v113, 0
	v_mov_b32_e32 v112, 0
	v_mov_b32_e32 v43, 0
	v_mov_b32_e32 v42, 0
	v_mov_b32_e32 v45, 0
	v_mov_b32_e32 v44, 0
	v_mov_b32_e32 v47, 0
	v_mov_b32_e32 v46, 0
	v_mov_b32_e32 v49, 0
	v_mov_b32_e32 v48, 0
	v_mov_b32_e32 v127, -1
	v_mov_b32_e32 v128, -1
	v_mov_b32_e32 v129, -1
	s_and_saveexec_b64 s[38:39], vcc
	s_cbranch_execz .LBB0_278
	v_mov_b32_e32 v21, v3
	v_lshlrev_b64 v[4:5], 11, v[20:21]
	v_lshl_add_u64 v[4:5], v[30:31], 0, v[4:5]
	global_load_dwordx2 v[42:43], v[4:5], off
	global_load_dwordx2 v[44:45], v[4:5], off offset:512
	global_load_dwordx2 v[46:47], v[4:5], off offset:1024
	global_load_dwordx2 v[48:49], v[4:5], off offset:1536
	s_nop 0
	v_cmp_lt_i32_e64 s[0:1], -1, v123
	s_and_b32 s30, s0, 0xffff
	s_mov_b32 s40, -1
	s_cmp_eq_u64 s[30:31], 0
	s_mov_b64 s[44:45], 0
	s_cbranch_scc1 .LBB0_269
	s_ff1_i32_b64 s1, s[30:31]
	v_readlane_b32 s42, v123, s1
	s_ashr_i32 s43, s42, 31
	s_lshl_b64 s[20:21], s[42:43], 11
	v_lshl_add_u64 v[4:5], v[32:33], 0, s[20:21]
	global_load_dwordx2 v[50:51], v[4:5], off
	global_load_dwordx2 v[52:53], v[4:5], off offset:512
	global_load_dwordx2 v[54:55], v[4:5], off offset:1024
	global_load_dwordx2 v[56:57], v[4:5], off offset:1536
	s_add_i32 s0, s0, -1
	s_and_b64 s[0:1], s[0:1], s[30:31]
	s_branch .LBB0_270

.LBB0_280:
	s_or_b64 exec, exec, s[0:1]
	v_cmp_lt_i32_e32 vcc, -1, v8
	v_mov_b32_e32 v4, v3
	v_mov_b32_e32 v5, v3
	v_mov_b32_e32 v6, v3
	v_mov_b32_e32 v7, v3
	v_mov_b32_e32 v8, v3
	v_mov_b32_e32 v9, v3
	v_mov_b32_e32 v10, v3
	v_mov_b32_e32 v11, v3
	v_mov_b32_e32 v12, v3
	v_mov_b32_e32 v13, v3
	v_mov_b32_e32 v14, v3
	v_mov_b32_e32 v15, v3
	v_mov_b32_e32 v16, v3
	v_mov_b32_e32 v17, v3
	v_mov_b32_e32 v2, v3
	v_mov_b64_e32 v[18:19], v[16:17]
	v_mov_b32_e32 v118, 0
	v_mov_b64_e32 v[16:17], v[14:15]
	v_mov_b64_e32 v[14:15], v[12:13]
	v_mov_b64_e32 v[12:13], v[10:11]
	v_mov_b64_e32 v[10:11], v[8:9]
	v_mov_b64_e32 v[8:9], v[6:7]
	v_mov_b64_e32 v[6:7], v[4:5]
	v_mov_b64_e32 v[4:5], v[2:3]
	v_mov_b32_e32 v119, 0
	v_mov_b32_e32 v120, 0
	v_mov_b32_e32 v121, 0
	s_and_saveexec_b64 s[0:1], vcc
	s_cbranch_execz .LBB0_285
	s_nop 0
	v_lshlrev_b32_e32 v16, 16, v94
	v_and_b32_e32 v17, 0xffff0000, v94
	v_lshlrev_b32_e32 v18, 16, v95
	v_and_b32_e32 v19, 0xffff0000, v95
	v_lshlrev_b32_e32 v4, 16, v104
	v_and_b32_e32 v5, 0xffff0000, v104
	v_lshlrev_b32_e32 v6, 16, v105
	v_and_b32_e32 v7, 0xffff0000, v105
	v_lshlrev_b32_e32 v8, 16, v102
	v_and_b32_e32 v9, 0xffff0000, v102
	v_lshlrev_b32_e32 v10, 16, v103
	v_and_b32_e32 v11, 0xffff0000, v103
	v_lshlrev_b32_e32 v12, 16, v98
	v_and_b32_e32 v13, 0xffff0000, v98
	v_lshlrev_b32_e32 v14, 16, v99
	v_and_b32_e32 v15, 0xffff0000, v99
	v_pk_add_f32 v[18:19], v[18:19], 0 op_sel_hi:[1,0]
	v_pk_add_f32 v[16:17], v[16:17], 0 op_sel_hi:[1,0]
	v_pk_add_f32 v[6:7], v[6:7], 0 op_sel_hi:[1,0]
	v_pk_add_f32 v[4:5], v[4:5], 0 op_sel_hi:[1,0]
	v_pk_add_f32 v[10:11], v[10:11], 0 op_sel_hi:[1,0]
	v_pk_add_f32 v[8:9], v[8:9], 0 op_sel_hi:[1,0]
	v_pk_add_f32 v[14:15], v[14:15], 0 op_sel_hi:[1,0]
	v_pk_add_f32 v[12:13], v[12:13], 0 op_sel_hi:[1,0]
	v_mov_b32_e32 v118, v16
	v_mov_b32_e32 v119, v17
	v_mov_b32_e32 v120, v18
	v_mov_b32_e32 v121, v19
	s_or_b64 exec, exec, s[0:1]
	v_cmp_lt_i32_e32 vcc, -1, v130
	s_and_saveexec_b64 s[0:1], vcc
	s_cbranch_execnz .LBB0_286

.LBB0_283:
	s_nop 0
	v_lshlrev_b32_e32 v80, 16, v92
	v_and_b32_e32 v81, 0xffff0000, v92
	v_lshlrev_b32_e32 v88, 16, v93
	v_and_b32_e32 v89, 0xffff0000, v93
	v_lshlrev_b32_e32 v92, 16, v90
	v_and_b32_e32 v93, 0xffff0000, v90
	v_lshlrev_b32_e32 v90, 16, v91
	v_and_b32_e32 v91, 0xffff0000, v91
	v_lshlrev_b32_e32 v94, 16, v86
	v_and_b32_e32 v95, 0xffff0000, v86
	v_lshlrev_b32_e32 v86, 16, v87
	v_and_b32_e32 v87, 0xffff0000, v87
	v_lshlrev_b32_e32 v96, 16, v66
	v_and_b32_e32 v97, 0xffff0000, v66
	v_lshlrev_b32_e32 v66, 16, v67
	v_and_b32_e32 v67, 0xffff0000, v67
	v_pk_add_f32 v[18:19], v[18:19], v[66:67]
	v_pk_add_f32 v[16:17], v[16:17], v[96:97]
	v_pk_add_f32 v[14:15], v[14:15], v[86:87]
	v_pk_add_f32 v[12:13], v[12:13], v[94:95]
	v_pk_add_f32 v[10:11], v[10:11], v[90:91]
	v_pk_add_f32 v[8:9], v[8:9], v[92:93]
	v_pk_add_f32 v[6:7], v[6:7], v[88:89]
	v_pk_add_f32 v[4:5], v[4:5], v[80:81]
	s_or_b64 exec, exec, s[0:1]
	v_cmp_lt_i32_e32 vcc, -1, v125
	s_and_saveexec_b64 s[0:1], vcc
	s_cbranch_execnz .LBB0_288

.LBB0_286:
	s_nop 0
	v_lshlrev_b32_e32 v16, 16, v100
	v_and_b32_e32 v17, 0xffff0000, v100
	v_lshlrev_b32_e32 v18, 16, v101
	v_and_b32_e32 v19, 0xffff0000, v101
	v_pk_add_f32 v[6:7], v[6:7], v[18:19]
	v_pk_add_f32 v[4:5], v[4:5], v[16:17]
	s_nop 0
	v_lshlrev_b32_e32 v16, 16, v96
	v_and_b32_e32 v17, 0xffff0000, v96
	v_lshlrev_b32_e32 v18, 16, v97
	v_and_b32_e32 v19, 0xffff0000, v97
	v_pk_add_f32 v[10:11], v[10:11], v[18:19]
	v_pk_add_f32 v[8:9], v[8:9], v[16:17]
	s_nop 0
	v_lshlrev_b32_e32 v16, 16, v88
	v_and_b32_e32 v17, 0xffff0000, v88
	v_lshlrev_b32_e32 v18, 16, v89
	v_and_b32_e32 v19, 0xffff0000, v89
	v_pk_add_f32 v[14:15], v[14:15], v[18:19]
	v_pk_add_f32 v[12:13], v[12:13], v[16:17]
	s_nop 0
	v_lshlrev_b32_e32 v16, 16, v80
	v_and_b32_e32 v17, 0xffff0000, v80
	v_lshlrev_b32_e32 v18, 16, v81
	v_and_b32_e32 v19, 0xffff0000, v81
	v_pk_add_f32 v[18:19], v[120:121], v[18:19]
	v_pk_add_f32 v[16:17], v[118:119], v[16:17]
	s_or_b64 exec, exec, s[0:1]
	v_cmp_lt_i32_e32 vcc, -1, v126
	s_and_saveexec_b64 s[0:1], vcc
	s_cbranch_execnz .LBB0_283

.LBB0_288:
	s_nop 0
	v_lshlrev_b32_e32 v66, 16, v74
	v_and_b32_e32 v67, 0xffff0000, v74
	v_lshlrev_b32_e32 v74, 16, v75
	v_and_b32_e32 v75, 0xffff0000, v75
	v_lshlrev_b32_e32 v80, 16, v76
	v_and_b32_e32 v81, 0xffff0000, v76
	v_lshlrev_b32_e32 v76, 16, v77
	v_and_b32_e32 v77, 0xffff0000, v77
	v_lshlrev_b32_e32 v86, 16, v72
	v_and_b32_e32 v87, 0xffff0000, v72
	v_lshlrev_b32_e32 v72, 16, v73
	v_and_b32_e32 v73, 0xffff0000, v73
	v_lshlrev_b32_e32 v88, 16, v70
	v_and_b32_e32 v89, 0xffff0000, v70
	v_lshlrev_b32_e32 v70, 16, v71
	v_and_b32_e32 v71, 0xffff0000, v71
	v_pk_add_f32 v[18:19], v[18:19], v[70:71]
	v_pk_add_f32 v[16:17], v[16:17], v[88:89]
	v_pk_add_f32 v[14:15], v[14:15], v[72:73]
	v_pk_add_f32 v[12:13], v[12:13], v[86:87]
	v_pk_add_f32 v[10:11], v[10:11], v[76:77]
	v_pk_add_f32 v[8:9], v[8:9], v[80:81]
	v_pk_add_f32 v[6:7], v[6:7], v[74:75]
	v_pk_add_f32 v[4:5], v[4:5], v[66:67]
	s_or_b64 exec, exec, s[0:1]
	v_cmp_ne_u64_e32 vcc, 0, v[38:39]
	s_and_saveexec_b64 s[38:39], vcc
	s_cbranch_execz .LBB0_265
